# grid barrier: L1 invalidate started by wave 1 at arrival, overlapping the barrier protocol (was issued and waited after the last poll)
# speedup vs baseline: 1.0137x; 1.0119x over previous
; __device__ __forceinline__ unsigned xb_ld(unsigned* p)              { return __hip_atomic_load(p, __ATOMIC_RELAXED, __HIP_MEMORY_SCOPE_AGENT); }
; __device__ __forceinline__ unsigned xb_add(unsigned* p, unsigned v) { return __hip_atomic_fetch_add(p, v, __ATOMIC_RELAXED, __HIP_MEMORY_SCOPE_AGENT); }
; #define XB_SPIN(cond, bar) do { unsigned _sp = 0; while (cond) { __builtin_amdgcn_s_sleep(1); \
;     if ((++_sp & 255u) == 0u) { if (xb_ld(&(bar)[XB_TMO])) break; if (_sp > XB_SPIN_CAP) { atomicAdd(&(bar)[XB_TMO], 1u); break; } } } } while (0)
; __device__ __forceinline__ void xcd_barrier(const XcdBarrier& b) {
;     asm volatile("s_waitcnt vmcnt(0)" ::: "memory");
;     __syncthreads();
;     if (threadIdx.x == 0) {
;         unsigned* bar = b.bar;
;         __builtin_amdgcn_s_waitcnt(0);
;         unsigned nloc = b.st[0], nx = b.st[1];
;         if (nloc == 0u) { xcd_barrier_complete(bar, b.x, nloc, nx); b.st[0] = nloc; b.st[1] = nx; }
;         const unsigned old = xb_add(&bar[XB_XSUB(b.x)], 1u);
;         const unsigned gen = old / nloc;
;         if (old + 1u == (gen + 1u) * nloc) {
;             __builtin_amdgcn_fence(__ATOMIC_RELEASE, "agent");
;             asm volatile("s_waitcnt vmcnt(0)" ::: "memory");
;             const unsigned og = xb_add(&bar[XB_TOP], 1u);
;             const unsigned tg = og / nx;
;             if (og + 1u == (tg + 1u) * nx) xb_add(&bar[XB_TOPGEN], 1u);
;             else XB_SPIN(xb_ld(&bar[XB_TOPGEN]) == tg, bar);
;             __builtin_amdgcn_fence(__ATOMIC_ACQUIRE, "agent");
;             xb_add(&bar[XB_XGEN(b.x)], 1u);
;             asm volatile("s_waitcnt vmcnt(0)" ::: "memory");
;         } else {
;             XB_SPIN(xb_ld(&bar[XB_XGEN(b.x)]) == gen, bar);
;             __builtin_amdgcn_fence(__ATOMIC_ACQUIRE, "agent");
;             asm volatile("s_waitcnt vmcnt(0)" ::: "memory");
;         }
;     }
;     __syncthreads();
.LBB0_93:
	s_cmp_lt_i32 s95, 3
	s_cbranch_scc1 .LBB0_143
	s_waitcnt vmcnt(0)
	v_cmp_eq_u32_e32 vcc, 0, v0
	s_waitcnt lgkmcnt(0)
	s_barrier
	v_readfirstlane_b32 s2, v0
	s_nop 3
	s_lshr_b32 s2, s2, 6
	s_cmp_lg_u32 s2, 1
	s_cbranch_scc1 .Lgb0_noinv
	buffer_inv sc1
.Lgb0_noinv:
	s_and_saveexec_b64 s[0:1], vcc
	s_cbranch_execz .LBB0_142
	v_readlane_b32 s4, v246, 22
	v_readlane_b32 s5, v246, 21
	s_waitcnt vmcnt(0) expcnt(0) lgkmcnt(0)
	s_nop 1
	v_mov_b32_e32 v1, s4
	ds_read_b32 v2, v1
	ds_read_b32 v3, v1 offset:4
	ds_read_b32 v4, v1 offset:8
	s_lshl_b32 s5, s5, 6
	s_add_u32 s6, s92, 0xf800
	s_addc_u32 s7, s93, 0
	s_add_u32 s8, s92, 0xfc00
	s_addc_u32 s9, s93, 0
	v_mov_b32_e32 v5, s5
	v_mov_b32_e32 v6, 1
	global_atomic_add v6, v5, v6, s[6:7] sc0
	s_waitcnt lgkmcnt(0)
	v_add_u32_e32 v4, 1, v4
	ds_write_b32 v1, v4 offset:8
	v_mul_lo_u32 v7, v4, v2
	s_waitcnt vmcnt(0)
	v_add_u32_e32 v6, 1, v6
	v_cmp_eq_u32_e32 vcc, v6, v7
	s_and_b64 vcc, exec, vcc
	s_cbranch_vccz .Lgb0_poll
	buffer_wbl2 sc1
	s_waitcnt vmcnt(0)
	s_lshr_b32 s5, s5, 4
	v_mov_b32_e32 v5, s5
	global_atomic_umax v5, v4, s[8:9]

; __device__ __forceinline__ unsigned xb_ld(unsigned* p)              { return __hip_atomic_load(p, __ATOMIC_RELAXED, __HIP_MEMORY_SCOPE_AGENT); }
; #define XB_SPIN(cond, bar) do { unsigned _sp = 0; while (cond) { __builtin_amdgcn_s_sleep(1); \
;     if ((++_sp & 255u) == 0u) { if (xb_ld(&(bar)[XB_TMO])) break; if (_sp > XB_SPIN_CAP) { atomicAdd(&(bar)[XB_TMO], 1u); break; } } } } while (0)
; __device__ __forceinline__ void xcd_barrier(const XcdBarrier& b) {
;     ...
;             XB_SPIN(xb_ld(&bar[XB_XGEN(b.x)]) == gen, bar);
;             __builtin_amdgcn_fence(__ATOMIC_ACQUIRE, "agent");
;             asm volatile("s_waitcnt vmcnt(0)" ::: "memory");
;         }
;     }
;     __syncthreads();
.Lgb0_done:
	s_waitcnt vmcnt(0) lgkmcnt(0)
.LBB0_142:
	s_or_b64 exec, exec, s[0:1]
	s_waitcnt vmcnt(0)
	s_waitcnt lgkmcnt(0)
	s_barrier

; __device__ __forceinline__ unsigned xb_ld(unsigned* p)              { return __hip_atomic_load(p, __ATOMIC_RELAXED, __HIP_MEMORY_SCOPE_AGENT); }
; __device__ __forceinline__ unsigned xb_add(unsigned* p, unsigned v) { return __hip_atomic_fetch_add(p, v, __ATOMIC_RELAXED, __HIP_MEMORY_SCOPE_AGENT); }
; #define XB_SPIN(cond, bar) do { unsigned _sp = 0; while (cond) { __builtin_amdgcn_s_sleep(1); \
;     if ((++_sp & 255u) == 0u) { if (xb_ld(&(bar)[XB_TMO])) break; if (_sp > XB_SPIN_CAP) { atomicAdd(&(bar)[XB_TMO], 1u); break; } } } } while (0)
; __device__ __forceinline__ void xcd_barrier(const XcdBarrier& b) {
;     asm volatile("s_waitcnt vmcnt(0)" ::: "memory");
;     __syncthreads();
;     if (threadIdx.x == 0) {
;         unsigned* bar = b.bar;
;         __builtin_amdgcn_s_waitcnt(0);
;         unsigned nloc = b.st[0], nx = b.st[1];
;         if (nloc == 0u) { xcd_barrier_complete(bar, b.x, nloc, nx); b.st[0] = nloc; b.st[1] = nx; }
;         const unsigned old = xb_add(&bar[XB_XSUB(b.x)], 1u);
;         const unsigned gen = old / nloc;
;         if (old + 1u == (gen + 1u) * nloc) {
;             __builtin_amdgcn_fence(__ATOMIC_RELEASE, "agent");
;             asm volatile("s_waitcnt vmcnt(0)" ::: "memory");
;             const unsigned og = xb_add(&bar[XB_TOP], 1u);
;             const unsigned tg = og / nx;
;             if (og + 1u == (tg + 1u) * nx) xb_add(&bar[XB_TOPGEN], 1u);
;             else XB_SPIN(xb_ld(&bar[XB_TOPGEN]) == tg, bar);
;             __builtin_amdgcn_fence(__ATOMIC_ACQUIRE, "agent");
;             xb_add(&bar[XB_XGEN(b.x)], 1u);
;             asm volatile("s_waitcnt vmcnt(0)" ::: "memory");
;         } else {
;             XB_SPIN(xb_ld(&bar[XB_XGEN(b.x)]) == gen, bar);
;             __builtin_amdgcn_fence(__ATOMIC_ACQUIRE, "agent");
;             asm volatile("s_waitcnt vmcnt(0)" ::: "memory");
;         }
;     }
;     __syncthreads();
.Lp3_after_pool:
	s_cmp_lt_i32 s95, 5
	s_cbranch_scc1 .LBB0_764
	s_waitcnt vmcnt(0)
	v_cmp_eq_u32_e32 vcc, 0, v0
	s_waitcnt vmcnt(0)
	s_barrier
	v_readfirstlane_b32 s2, v0
	s_nop 3
	s_lshr_b32 s2, s2, 6
	s_cmp_lg_u32 s2, 1
	s_cbranch_scc1 .Lgb1_noinv
	buffer_inv sc1

; __device__ __forceinline__ unsigned xb_ld(unsigned* p)              { return __hip_atomic_load(p, __ATOMIC_RELAXED, __HIP_MEMORY_SCOPE_AGENT); }
; __device__ __forceinline__ unsigned xb_add(unsigned* p, unsigned v) { return __hip_atomic_fetch_add(p, v, __ATOMIC_RELAXED, __HIP_MEMORY_SCOPE_AGENT); }
; #define XB_SPIN(cond, bar) do { unsigned _sp = 0; while (cond) { __builtin_amdgcn_s_sleep(1); \
;     if ((++_sp & 255u) == 0u) { if (xb_ld(&(bar)[XB_TMO])) break; if (_sp > XB_SPIN_CAP) { atomicAdd(&(bar)[XB_TMO], 1u); break; } } } } while (0)
; __device__ __forceinline__ void xcd_barrier(const XcdBarrier& b) {
;     asm volatile("s_waitcnt vmcnt(0)" ::: "memory");
;     __syncthreads();
;     if (threadIdx.x == 0) {
;         unsigned* bar = b.bar;
;         __builtin_amdgcn_s_waitcnt(0);
;         unsigned nloc = b.st[0], nx = b.st[1];
;         if (nloc == 0u) { xcd_barrier_complete(bar, b.x, nloc, nx); b.st[0] = nloc; b.st[1] = nx; }
;         const unsigned old = xb_add(&bar[XB_XSUB(b.x)], 1u);
;         const unsigned gen = old / nloc;
;         if (old + 1u == (gen + 1u) * nloc) {
;             __builtin_amdgcn_fence(__ATOMIC_RELEASE, "agent");
;             asm volatile("s_waitcnt vmcnt(0)" ::: "memory");
;             const unsigned og = xb_add(&bar[XB_TOP], 1u);
;             const unsigned tg = og / nx;
;             if (og + 1u == (tg + 1u) * nx) xb_add(&bar[XB_TOPGEN], 1u);
;             else XB_SPIN(xb_ld(&bar[XB_TOPGEN]) == tg, bar);
;             __builtin_amdgcn_fence(__ATOMIC_ACQUIRE, "agent");
;             xb_add(&bar[XB_XGEN(b.x)], 1u);
;             asm volatile("s_waitcnt vmcnt(0)" ::: "memory");
;         } else {
;             XB_SPIN(xb_ld(&bar[XB_XGEN(b.x)]) == gen, bar);
;             __builtin_amdgcn_fence(__ATOMIC_ACQUIRE, "agent");
;             asm volatile("s_waitcnt vmcnt(0)" ::: "memory");
;         }
;     }
;     __syncthreads();
.LBB0_871:
	s_cmp_lt_i32 s95, 6
	s_cbranch_scc1 .LBB0_921
	s_waitcnt vmcnt(0)
	v_cmp_eq_u32_e32 vcc, 0, v0
	s_waitcnt vmcnt(0)
	s_barrier
	v_readfirstlane_b32 s2, v0
	s_nop 3
	s_lshr_b32 s2, s2, 6
	s_cmp_lg_u32 s2, 1
	s_cbranch_scc1 .Lgb2_noinv
	buffer_inv sc1

; __device__ __forceinline__ unsigned xb_ld(unsigned* p)              { return __hip_atomic_load(p, __ATOMIC_RELAXED, __HIP_MEMORY_SCOPE_AGENT); }
; __device__ __forceinline__ unsigned xb_add(unsigned* p, unsigned v) { return __hip_atomic_fetch_add(p, v, __ATOMIC_RELAXED, __HIP_MEMORY_SCOPE_AGENT); }
; #define XB_SPIN(cond, bar) do { unsigned _sp = 0; while (cond) { __builtin_amdgcn_s_sleep(1); \
;     if ((++_sp & 255u) == 0u) { if (xb_ld(&(bar)[XB_TMO])) break; if (_sp > XB_SPIN_CAP) { atomicAdd(&(bar)[XB_TMO], 1u); break; } } } } while (0)
; __device__ __forceinline__ void xcd_barrier(const XcdBarrier& b) {
;     asm volatile("s_waitcnt vmcnt(0)" ::: "memory");
;     __syncthreads();
;     if (threadIdx.x == 0) {
;         unsigned* bar = b.bar;
;         __builtin_amdgcn_s_waitcnt(0);
;         unsigned nloc = b.st[0], nx = b.st[1];
;         if (nloc == 0u) { xcd_barrier_complete(bar, b.x, nloc, nx); b.st[0] = nloc; b.st[1] = nx; }
;         const unsigned old = xb_add(&bar[XB_XSUB(b.x)], 1u);
;         const unsigned gen = old / nloc;
;         if (old + 1u == (gen + 1u) * nloc) {
;             __builtin_amdgcn_fence(__ATOMIC_RELEASE, "agent");
;             asm volatile("s_waitcnt vmcnt(0)" ::: "memory");
;             const unsigned og = xb_add(&bar[XB_TOP], 1u);
;             const unsigned tg = og / nx;
;             if (og + 1u == (tg + 1u) * nx) xb_add(&bar[XB_TOPGEN], 1u);
;             else XB_SPIN(xb_ld(&bar[XB_TOPGEN]) == tg, bar);
;             __builtin_amdgcn_fence(__ATOMIC_ACQUIRE, "agent");
;             xb_add(&bar[XB_XGEN(b.x)], 1u);
;             asm volatile("s_waitcnt vmcnt(0)" ::: "memory");
;         } else {
;             XB_SPIN(xb_ld(&bar[XB_XGEN(b.x)]) == gen, bar);
;             __builtin_amdgcn_fence(__ATOMIC_ACQUIRE, "agent");
;             asm volatile("s_waitcnt vmcnt(0)" ::: "memory");
;         }
;     }
;     __syncthreads();
.LBB0_953:
	s_cmp_lt_i32 s95, 7
	s_cbranch_scc1 .LBB0_1003
	s_waitcnt vmcnt(0)
	v_cmp_eq_u32_e32 vcc, 0, v0
	s_waitcnt vmcnt(0) lgkmcnt(0)
	s_barrier
	v_readfirstlane_b32 s2, v0
	s_nop 3
	s_lshr_b32 s2, s2, 6
	s_cmp_lg_u32 s2, 1
	s_cbranch_scc1 .Lgb3_noinv
	buffer_inv sc1

; __device__ __forceinline__ unsigned xb_ld(unsigned* p)              { return __hip_atomic_load(p, __ATOMIC_RELAXED, __HIP_MEMORY_SCOPE_AGENT); }
; __device__ __forceinline__ unsigned xb_add(unsigned* p, unsigned v) { return __hip_atomic_fetch_add(p, v, __ATOMIC_RELAXED, __HIP_MEMORY_SCOPE_AGENT); }
; #define XB_SPIN(cond, bar) do { unsigned _sp = 0; while (cond) { __builtin_amdgcn_s_sleep(1); \
;     if ((++_sp & 255u) == 0u) { if (xb_ld(&(bar)[XB_TMO])) break; if (_sp > XB_SPIN_CAP) { atomicAdd(&(bar)[XB_TMO], 1u); break; } } } } while (0)
; __device__ __forceinline__ void xcd_barrier(const XcdBarrier& b) {
;     asm volatile("s_waitcnt vmcnt(0)" ::: "memory");
;     __syncthreads();
;     if (threadIdx.x == 0) {
;         unsigned* bar = b.bar;
;         __builtin_amdgcn_s_waitcnt(0);
;         unsigned nloc = b.st[0], nx = b.st[1];
;         if (nloc == 0u) { xcd_barrier_complete(bar, b.x, nloc, nx); b.st[0] = nloc; b.st[1] = nx; }
;         const unsigned old = xb_add(&bar[XB_XSUB(b.x)], 1u);
;         const unsigned gen = old / nloc;
;         if (old + 1u == (gen + 1u) * nloc) {
;             __builtin_amdgcn_fence(__ATOMIC_RELEASE, "agent");
;             asm volatile("s_waitcnt vmcnt(0)" ::: "memory");
;             const unsigned og = xb_add(&bar[XB_TOP], 1u);
;             const unsigned tg = og / nx;
;             if (og + 1u == (tg + 1u) * nx) xb_add(&bar[XB_TOPGEN], 1u);
;             else XB_SPIN(xb_ld(&bar[XB_TOPGEN]) == tg, bar);
;             __builtin_amdgcn_fence(__ATOMIC_ACQUIRE, "agent");
;             xb_add(&bar[XB_XGEN(b.x)], 1u);
;             asm volatile("s_waitcnt vmcnt(0)" ::: "memory");
;         } else {
;             XB_SPIN(xb_ld(&bar[XB_XGEN(b.x)]) == gen, bar);
;             __builtin_amdgcn_fence(__ATOMIC_ACQUIRE, "agent");
;             asm volatile("s_waitcnt vmcnt(0)" ::: "memory");
;         }
;     }
;     __syncthreads();
.LBB0_1030:
	s_cmp_lt_i32 s95, 8
	s_cbranch_scc1 .LBB0_1080
	s_waitcnt vmcnt(0)
	v_cmp_eq_u32_e32 vcc, 0, v0
	s_waitcnt vmcnt(0) lgkmcnt(0)
	s_barrier
	v_readfirstlane_b32 s2, v0
	s_nop 3
	s_lshr_b32 s2, s2, 6
	s_cmp_lg_u32 s2, 1
	s_cbranch_scc1 .Lgb4_noinv
	buffer_inv sc1

; __device__ __forceinline__ unsigned xb_ld(unsigned* p)              { return __hip_atomic_load(p, __ATOMIC_RELAXED, __HIP_MEMORY_SCOPE_AGENT); }
; __device__ __forceinline__ unsigned xb_add(unsigned* p, unsigned v) { return __hip_atomic_fetch_add(p, v, __ATOMIC_RELAXED, __HIP_MEMORY_SCOPE_AGENT); }
; #define XB_SPIN(cond, bar) do { unsigned _sp = 0; while (cond) { __builtin_amdgcn_s_sleep(1); \
;     if ((++_sp & 255u) == 0u) { if (xb_ld(&(bar)[XB_TMO])) break; if (_sp > XB_SPIN_CAP) { atomicAdd(&(bar)[XB_TMO], 1u); break; } } } } while (0)
; __device__ __forceinline__ void xcd_barrier(const XcdBarrier& b) {
;     asm volatile("s_waitcnt vmcnt(0)" ::: "memory");
;     __syncthreads();
;     if (threadIdx.x == 0) {
;         unsigned* bar = b.bar;
;         __builtin_amdgcn_s_waitcnt(0);
;         unsigned nloc = b.st[0], nx = b.st[1];
;         if (nloc == 0u) { xcd_barrier_complete(bar, b.x, nloc, nx); b.st[0] = nloc; b.st[1] = nx; }
;         const unsigned old = xb_add(&bar[XB_XSUB(b.x)], 1u);
;         const unsigned gen = old / nloc;
;         if (old + 1u == (gen + 1u) * nloc) {
;             __builtin_amdgcn_fence(__ATOMIC_RELEASE, "agent");
;             asm volatile("s_waitcnt vmcnt(0)" ::: "memory");
;             const unsigned og = xb_add(&bar[XB_TOP], 1u);
;             const unsigned tg = og / nx;
;             if (og + 1u == (tg + 1u) * nx) xb_add(&bar[XB_TOPGEN], 1u);
;             else XB_SPIN(xb_ld(&bar[XB_TOPGEN]) == tg, bar);
;             __builtin_amdgcn_fence(__ATOMIC_ACQUIRE, "agent");
;             xb_add(&bar[XB_XGEN(b.x)], 1u);
;             asm volatile("s_waitcnt vmcnt(0)" ::: "memory");
;         } else {
;             XB_SPIN(xb_ld(&bar[XB_XGEN(b.x)]) == gen, bar);
;             __builtin_amdgcn_fence(__ATOMIC_ACQUIRE, "agent");
;             asm volatile("s_waitcnt vmcnt(0)" ::: "memory");
;         }
;     }
;     __syncthreads();
.LBB0_1102:
	s_cmp_lt_i32 s95, 9
	s_cbranch_scc1 .LBB0_1152
	s_waitcnt vmcnt(0)
	v_cmp_eq_u32_e32 vcc, 0, v0
	s_waitcnt vmcnt(0) lgkmcnt(0)
	s_barrier
	v_readfirstlane_b32 s2, v0
	s_nop 3
	s_lshr_b32 s2, s2, 6
	s_cmp_lg_u32 s2, 1
	s_cbranch_scc1 .Lgb5_noinv
	buffer_inv sc1

; __device__ __forceinline__ unsigned xb_ld(unsigned* p)              { return __hip_atomic_load(p, __ATOMIC_RELAXED, __HIP_MEMORY_SCOPE_AGENT); }
; __device__ __forceinline__ unsigned xb_add(unsigned* p, unsigned v) { return __hip_atomic_fetch_add(p, v, __ATOMIC_RELAXED, __HIP_MEMORY_SCOPE_AGENT); }
; #define XB_SPIN(cond, bar) do { unsigned _sp = 0; while (cond) { __builtin_amdgcn_s_sleep(1); \
;     if ((++_sp & 255u) == 0u) { if (xb_ld(&(bar)[XB_TMO])) break; if (_sp > XB_SPIN_CAP) { atomicAdd(&(bar)[XB_TMO], 1u); break; } } } } while (0)
; __device__ __forceinline__ void xcd_barrier(const XcdBarrier& b) {
;     asm volatile("s_waitcnt vmcnt(0)" ::: "memory");
;     __syncthreads();
;     if (threadIdx.x == 0) {
;         unsigned* bar = b.bar;
;         __builtin_amdgcn_s_waitcnt(0);
;         unsigned nloc = b.st[0], nx = b.st[1];
;         if (nloc == 0u) { xcd_barrier_complete(bar, b.x, nloc, nx); b.st[0] = nloc; b.st[1] = nx; }
;         const unsigned old = xb_add(&bar[XB_XSUB(b.x)], 1u);
;         const unsigned gen = old / nloc;
;         if (old + 1u == (gen + 1u) * nloc) {
;             __builtin_amdgcn_fence(__ATOMIC_RELEASE, "agent");
;             asm volatile("s_waitcnt vmcnt(0)" ::: "memory");
;             const unsigned og = xb_add(&bar[XB_TOP], 1u);
;             const unsigned tg = og / nx;
;             if (og + 1u == (tg + 1u) * nx) xb_add(&bar[XB_TOPGEN], 1u);
;             else XB_SPIN(xb_ld(&bar[XB_TOPGEN]) == tg, bar);
;             __builtin_amdgcn_fence(__ATOMIC_ACQUIRE, "agent");
;             xb_add(&bar[XB_XGEN(b.x)], 1u);
;             asm volatile("s_waitcnt vmcnt(0)" ::: "memory");
;         } else {
;             XB_SPIN(xb_ld(&bar[XB_XGEN(b.x)]) == gen, bar);
;             __builtin_amdgcn_fence(__ATOMIC_ACQUIRE, "agent");
;             asm volatile("s_waitcnt vmcnt(0)" ::: "memory");
;         }
;     }
;     __syncthreads();
.LBB0_1228:
	s_cmp_lt_i32 s95, 10
	v_readlane_b32 s97, v246, 24
	s_cbranch_scc1 .LBB0_1278
	s_waitcnt vmcnt(0)
	v_cmp_eq_u32_e32 vcc, 0, v0
	s_waitcnt vmcnt(0) lgkmcnt(0)
	s_barrier
	v_readfirstlane_b32 s2, v0
	s_nop 3
	s_lshr_b32 s2, s2, 6
	s_cmp_lg_u32 s2, 1
	s_cbranch_scc1 .Lgb6_noinv
	buffer_inv sc1
.Lgb6_noinv:
	s_and_saveexec_b64 s[0:1], vcc
	v_readlane_b32 s46, v246, 22
	s_cbranch_execz .LBB0_1277
	v_readlane_b32 s4, v246, 22
	v_readlane_b32 s5, v246, 21
	s_waitcnt vmcnt(0) expcnt(0) lgkmcnt(0)
	s_nop 1
	v_mov_b32_e32 v1, s4
	ds_read_b32 v2, v1
	ds_read_b32 v3, v1 offset:4
	ds_read_b32 v4, v1 offset:8
	s_lshl_b32 s5, s5, 6
	s_add_u32 s6, s92, 0xf800
	s_addc_u32 s7, s93, 0
	s_add_u32 s8, s92, 0xfc00
	s_addc_u32 s9, s93, 0
	v_mov_b32_e32 v5, s5
	v_mov_b32_e32 v6, 1
	global_atomic_add v6, v5, v6, s[6:7] sc0
	s_waitcnt lgkmcnt(0)
	v_add_u32_e32 v4, 1, v4
	ds_write_b32 v1, v4 offset:8
	v_mul_lo_u32 v7, v4, v2
	s_waitcnt vmcnt(0)
	v_add_u32_e32 v6, 1, v6
	v_cmp_eq_u32_e32 vcc, v6, v7
	s_and_b64 vcc, exec, vcc
	s_cbranch_vccz .Lgb6_poll
	buffer_wbl2 sc1
	s_waitcnt vmcnt(0)
	s_lshr_b32 s5, s5, 4
	v_mov_b32_e32 v5, s5
	global_atomic_umax v5, v4, s[8:9]

; __device__ __forceinline__ unsigned xb_ld(unsigned* p)              { return __hip_atomic_load(p, __ATOMIC_RELAXED, __HIP_MEMORY_SCOPE_AGENT); }
; __device__ __forceinline__ unsigned xb_add(unsigned* p, unsigned v) { return __hip_atomic_fetch_add(p, v, __ATOMIC_RELAXED, __HIP_MEMORY_SCOPE_AGENT); }
; #define XB_SPIN(cond, bar) do { unsigned _sp = 0; while (cond) { __builtin_amdgcn_s_sleep(1); \
;     if ((++_sp & 255u) == 0u) { if (xb_ld(&(bar)[XB_TMO])) break; if (_sp > XB_SPIN_CAP) { atomicAdd(&(bar)[XB_TMO], 1u); break; } } } } while (0)
; __device__ __forceinline__ void xcd_barrier(const XcdBarrier& b) {
;     asm volatile("s_waitcnt vmcnt(0)" ::: "memory");
;     __syncthreads();
;     if (threadIdx.x == 0) {
;         unsigned* bar = b.bar;
;         __builtin_amdgcn_s_waitcnt(0);
;         unsigned nloc = b.st[0], nx = b.st[1];
;         if (nloc == 0u) { xcd_barrier_complete(bar, b.x, nloc, nx); b.st[0] = nloc; b.st[1] = nx; }
;         const unsigned old = xb_add(&bar[XB_XSUB(b.x)], 1u);
;         const unsigned gen = old / nloc;
;         if (old + 1u == (gen + 1u) * nloc) {
;             __builtin_amdgcn_fence(__ATOMIC_RELEASE, "agent");
;             asm volatile("s_waitcnt vmcnt(0)" ::: "memory");
;             const unsigned og = xb_add(&bar[XB_TOP], 1u);
;             const unsigned tg = og / nx;
;             if (og + 1u == (tg + 1u) * nx) xb_add(&bar[XB_TOPGEN], 1u);
;             else XB_SPIN(xb_ld(&bar[XB_TOPGEN]) == tg, bar);
;             __builtin_amdgcn_fence(__ATOMIC_ACQUIRE, "agent");
;             xb_add(&bar[XB_XGEN(b.x)], 1u);
;             asm volatile("s_waitcnt vmcnt(0)" ::: "memory");
;         } else {
;             XB_SPIN(xb_ld(&bar[XB_XGEN(b.x)]) == gen, bar);
;             __builtin_amdgcn_fence(__ATOMIC_ACQUIRE, "agent");
;             asm volatile("s_waitcnt vmcnt(0)" ::: "memory");
;         }
;     }
;     __syncthreads();
.LBB0_1321:
	s_cmp_lt_i32 s95, 11
	s_cbranch_scc1 .LBB0_1371
	s_waitcnt vmcnt(0)
	v_cmp_eq_u32_e32 vcc, 0, v0
	s_waitcnt vmcnt(0) lgkmcnt(0)
	s_barrier
	v_readfirstlane_b32 s2, v0
	s_nop 3
	s_lshr_b32 s2, s2, 6
	s_cmp_lg_u32 s2, 1
	s_cbranch_scc1 .Lgb7_noinv
	buffer_inv sc1

; __device__ __forceinline__ unsigned xb_ld(unsigned* p)              { return __hip_atomic_load(p, __ATOMIC_RELAXED, __HIP_MEMORY_SCOPE_AGENT); }
; __device__ __forceinline__ unsigned xb_add(unsigned* p, unsigned v) { return __hip_atomic_fetch_add(p, v, __ATOMIC_RELAXED, __HIP_MEMORY_SCOPE_AGENT); }
; #define XB_SPIN(cond, bar) do { unsigned _sp = 0; while (cond) { __builtin_amdgcn_s_sleep(1); \
;     if ((++_sp & 255u) == 0u) { if (xb_ld(&(bar)[XB_TMO])) break; if (_sp > XB_SPIN_CAP) { atomicAdd(&(bar)[XB_TMO], 1u); break; } } } } while (0)
; __device__ __forceinline__ void xcd_barrier(const XcdBarrier& b) {
;     asm volatile("s_waitcnt vmcnt(0)" ::: "memory");
;     __syncthreads();
;     if (threadIdx.x == 0) {
;         unsigned* bar = b.bar;
;         __builtin_amdgcn_s_waitcnt(0);
;         unsigned nloc = b.st[0], nx = b.st[1];
;         if (nloc == 0u) { xcd_barrier_complete(bar, b.x, nloc, nx); b.st[0] = nloc; b.st[1] = nx; }
;         const unsigned old = xb_add(&bar[XB_XSUB(b.x)], 1u);
;         const unsigned gen = old / nloc;
;         if (old + 1u == (gen + 1u) * nloc) {
;             __builtin_amdgcn_fence(__ATOMIC_RELEASE, "agent");
;             asm volatile("s_waitcnt vmcnt(0)" ::: "memory");
;             const unsigned og = xb_add(&bar[XB_TOP], 1u);
;             const unsigned tg = og / nx;
;             if (og + 1u == (tg + 1u) * nx) xb_add(&bar[XB_TOPGEN], 1u);
;             else XB_SPIN(xb_ld(&bar[XB_TOPGEN]) == tg, bar);
;             __builtin_amdgcn_fence(__ATOMIC_ACQUIRE, "agent");
;             xb_add(&bar[XB_XGEN(b.x)], 1u);
;             asm volatile("s_waitcnt vmcnt(0)" ::: "memory");
;         } else {
;             XB_SPIN(xb_ld(&bar[XB_XGEN(b.x)]) == gen, bar);
;             __builtin_amdgcn_fence(__ATOMIC_ACQUIRE, "agent");
;             asm volatile("s_waitcnt vmcnt(0)" ::: "memory");
;         }
;     }
;     __syncthreads();
.LBB0_1412:
	s_cmp_lt_i32 s95, 12
	s_cbranch_scc1 .LBB0_1462
	s_waitcnt vmcnt(0)
	v_cmp_eq_u32_e32 vcc, 0, v0
	s_waitcnt vmcnt(0) lgkmcnt(0)
	s_barrier
	v_readfirstlane_b32 s2, v0
	s_nop 3
	s_lshr_b32 s2, s2, 6
	s_cmp_lg_u32 s2, 1
	s_cbranch_scc1 .Lgb8_noinv
	buffer_inv sc1
